# speedup vs baseline: 1.0125x; 1.0125x over previous
_Z13gemm2b_kernelPKDF16_S0_PfPKf:
	v_lshrrev_b32_e32 v1, 4, v0
	s_load_dwordx8 s[4:11], s[0:1], 0x0
	s_ashr_i32 s14, s2, 3
	s_lshl_b32 s0, s2, 5
	v_xor_b32_e32 v2, v1, v0
	s_and_b32 s0, s0, 0xe0
	s_lshl_b32 s1, s14, 7
	v_lshlrev_b32_e32 v2, 3, v2
	s_add_i32 s0, s0, s14
	s_and_b32 s12, s1, 0x380
	v_and_b32_e32 v2, 56, v2
	v_lshlrev_b32_e32 v3, 8, v0
	s_mov_b32 s1, 0x1f800
	s_lshl_b32 s0, s0, 5
	v_and_or_b32 v4, v3, s1, v2
	v_or_b32_e32 v5, 0x20000, v3
	s_mov_b32 s1, 0x3f800
	v_and_or_b32 v6, v5, s1, v2
	v_or_b32_e32 v8, 0x60000, v3
	s_mov_b32 s1, 0x7f800
	s_and_b32 s0, s0, 0xffffff00
	v_and_or_b32 v2, v8, s1, v2
	s_ashr_i32 s1, s0, 31
	s_lshl_b64 s[2:3], s[0:1], 12
	v_lshl_add_u32 v76, v0, 4, 0
	s_waitcnt lgkmcnt(0)
	s_add_u32 s2, s4, s2
	v_readfirstlane_b32 s1, v76
	v_add_u32_e32 v11, 0x2000, v76
	v_lshlrev_b32_e32 v4, 1, v4
	s_addc_u32 s3, s5, s3
	s_mov_b32 m0, s1
	v_readfirstlane_b32 s1, v11
	v_add_u32_e32 v11, 0x4000, v76
	v_lshlrev_b32_e32 v6, 1, v6
	global_load_lds_dwordx4 v4, s[2:3]
	s_mov_b32 m0, s1
	v_readfirstlane_b32 s1, v11
	v_or_b32_e32 v7, 0x80000, v4
	global_load_lds_dwordx4 v6, s[2:3]
	s_mov_b32 m0, s1
	v_lshlrev_b32_e32 v2, 1, v2
	global_load_lds_dwordx4 v7, s[2:3]
	v_add_u32_e32 v7, 0x6000, v76
	v_bfe_u32 v9, v0, 1, 3
	v_readfirstlane_b32 s1, v7
	s_mov_b32 m0, s1
	s_lshl_b32 s1, s12, 12
	global_load_lds_dwordx4 v2, s[2:3]
	v_add_u32_e32 v2, 0x8000, v76
	s_add_u32 s4, s6, s1
	v_readfirstlane_b32 s1, v2
	v_add_u32_e32 v2, 0xa000, v76
	s_addc_u32 s5, s7, 0
	s_mov_b32 m0, s1
	v_readfirstlane_b32 s1, v2
	global_load_lds_dwordx4 v4, s[4:5]
	s_mov_b32 m0, s1
	v_bitop3_b32 v9, v1, v9, 3 bitop3:0x6c
	global_load_lds_dwordx4 v6, s[4:5]
	s_lshl_b32 s1, s14, 19
	v_bitop3_b32 v1, v1, 7, v0 bitop3:0x48
	v_and_b32_e32 v80, 15, v0
	s_and_b32 s1, s1, 0x380000
	v_lshlrev_b32_e32 v2, 1, v5
	v_lshlrev_b32_e32 v6, 4, v1
	s_mov_b32 s4, 0x7f000
	v_bfe_u32 v82, v0, 6, 1
	v_lshrrev_b32_e32 v81, 7, v0
	v_lshlrev_b32_e32 v3, 7, v80
	v_and_or_b32 v4, v2, s4, v6
	s_add_u32 s4, s6, s1
	v_bfe_u32 v83, v0, 4, 2
	v_lshl_or_b32 v3, v9, 4, v3
	v_lshlrev_b32_e32 v9, 13, v81
	v_lshlrev_b32_e32 v10, 13, v82
	v_mov_b32_e32 v5, 0
	s_addc_u32 s5, s7, 0
	v_lshlrev_b32_e32 v0, 9, v0
	s_mov_b32 s1, 0x3f000
	v_or_b32_e32 v84, v3, v10
	v_or_b32_e32 v77, v3, v9
	v_bitop3_b32 v85, v3, 64, v9 bitop3:0x36
	v_bitop3_b32 v78, v3, 64, v10 bitop3:0x36
	v_lshl_add_u64 v[2:3], s[4:5], 0, v[4:5]
	s_mov_b64 s[6:7], 0x80
	v_and_or_b32 v0, v0, s1, v6
	v_mov_b32_e32 v1, v5
	v_lshl_add_u64 v[64:65], v[2:3], 0, s[6:7]
	v_lshl_add_u64 v[2:3], s[4:5], 0, v[0:1]
	v_lshl_add_u64 v[66:67], v[2:3], 0, s[6:7]
	v_lshlrev_b32_e32 v2, 1, v8
	s_mov_b32 s1, 0xff000
	v_and_or_b32 v2, v2, s1, v6
	v_mov_b32_e32 v3, v5
	v_lshl_add_u64 v[2:3], s[2:3], 0, v[2:3]
	v_lshl_add_u64 v[68:69], v[2:3], 0, s[6:7]
	v_or_b32_e32 v2, 0x80000, v0
	v_mov_b32_e32 v3, v5
	v_lshl_add_u64 v[2:3], s[2:3], 0, v[2:3]
	v_lshl_add_u64 v[70:71], v[2:3], 0, s[6:7]
	v_lshl_add_u64 v[2:3], s[2:3], 0, v[4:5]
	v_lshl_add_u64 v[0:1], s[2:3], 0, v[0:1]
	s_mov_b32 s13, 1
	v_lshl_add_u64 v[72:73], v[2:3], 0, s[6:7]
	v_lshl_add_u64 v[74:75], v[0:1], 0, s[6:7]
	s_mov_b64 s[2:3], 0
	v_mov_b32_e32 v4, v5
	v_mov_b32_e32 v6, v5
	v_mov_b32_e32 v7, v5
	v_mov_b32_e32 v0, v5
	v_mov_b32_e32 v1, v5
	v_mov_b32_e32 v2, v5
	v_mov_b32_e32 v3, v5
	v_mov_b32_e32 v8, v5
	v_mov_b32_e32 v9, v5
	v_mov_b32_e32 v10, v5
	v_mov_b32_e32 v11, v5
	v_mov_b32_e32 v12, v5
	v_mov_b32_e32 v13, v5
	v_mov_b32_e32 v14, v5
	v_mov_b32_e32 v15, v5
	v_mov_b32_e32 v16, v5
	v_mov_b32_e32 v17, v5
	v_mov_b32_e32 v18, v5
	v_mov_b32_e32 v19, v5
	v_mov_b32_e32 v20, v5
	v_mov_b32_e32 v21, v5
	v_mov_b32_e32 v22, v5
	v_mov_b32_e32 v23, v5
	v_mov_b32_e32 v24, v5
	v_mov_b32_e32 v25, v5
	v_mov_b32_e32 v26, v5
	v_mov_b32_e32 v27, v5
	v_mov_b32_e32 v28, v5
	v_mov_b32_e32 v29, v5
	v_mov_b32_e32 v30, v5
	v_mov_b32_e32 v31, v5
	v_mov_b32_e32 v32, v5
	v_mov_b32_e32 v33, v5
	v_mov_b32_e32 v34, v5
	v_mov_b32_e32 v35, v5
	v_mov_b32_e32 v36, v5
	v_mov_b32_e32 v37, v5
	v_mov_b32_e32 v38, v5
	v_mov_b32_e32 v39, v5
	v_mov_b32_e32 v40, v5
	v_mov_b32_e32 v41, v5
	v_mov_b32_e32 v42, v5
	v_mov_b32_e32 v43, v5
	v_mov_b32_e32 v44, v5
	v_mov_b32_e32 v45, v5
	v_mov_b32_e32 v46, v5
	v_mov_b32_e32 v47, v5
	v_mov_b32_e32 v48, v5
	v_mov_b32_e32 v49, v5
	v_mov_b32_e32 v50, v5
	v_mov_b32_e32 v51, v5
	v_mov_b32_e32 v52, v5
	v_mov_b32_e32 v53, v5
	v_mov_b32_e32 v54, v5
	v_mov_b32_e32 v55, v5
	v_mov_b32_e32 v56, v5
	v_mov_b32_e32 v57, v5
	v_mov_b32_e32 v58, v5
	v_mov_b32_e32 v59, v5
	v_mov_b32_e32 v60, v5
	v_mov_b32_e32 v61, v5
	v_mov_b32_e32 v62, v5
	v_mov_b32_e32 v63, v5
	v_add_u32_e32 v79, 0xc000, v76
	s_mov_b32 s16, 0x18000
	s_mov_b32 s17, 0
	v_readfirstlane_b32 s18, v76
	v_readfirstlane_b32 s4, v79
	v_add_u32_e32 v98, 0x2000, v79
	v_lshl_add_u64 v[86:87], v[74:75], 0, s[2:3]
	v_add_u32_e32 v99, 0x4000, v79
	v_readfirstlane_b32 s5, v98
	s_mov_b32 m0, s4
	v_lshl_add_u64 v[88:89], v[72:73], 0, s[2:3]
	v_add_u32_e32 v100, 0x6000, v79
	v_readfirstlane_b32 s6, v99
	global_load_lds_dwordx4 v[86:87], off
	s_mov_b32 m0, s5
	v_lshl_add_u64 v[90:91], v[70:71], 0, s[2:3]
	v_add_u32_e32 v101, 0x8000, v79
	v_readfirstlane_b32 s7, v100
	global_load_lds_dwordx4 v[88:89], off
	s_mov_b32 m0, s6
	v_lshl_add_u64 v[92:93], v[68:69], 0, s[2:3]
	v_add_u32_e32 v79, 0xa000, v79
	v_readfirstlane_b32 s14, v101
	global_load_lds_dwordx4 v[90:91], off
	s_mov_b32 m0, s7
	v_lshl_add_u64 v[94:95], v[66:67], 0, s[2:3]
	v_readfirstlane_b32 s15, v79
	global_load_lds_dwordx4 v[92:93], off
	s_mov_b32 m0, s14
	v_lshl_add_u64 v[96:97], v[64:65], 0, s[2:3]
	global_load_lds_dwordx4 v[94:95], off
	s_mov_b32 m0, s15
	s_nop 0
	global_load_lds_dwordx4 v[96:97], off
	s_mov_b64 s[2:3], 0x80
.LBB1_1:
	s_add_i32 s1, s17, 0
	s_add_u32 s19, s18, s16
	s_add_u32 s20, s19, 0x2000
	s_add_u32 s21, s19, 0x4000
	s_add_u32 s22, s19, 0x6000
	s_add_u32 s23, s19, 0x8000
	s_add_u32 s24, s19, 0xa000
	s_add_i32 s16, s16, 0xc000
	s_cmp_eq_u32 s16, 0x24000
	s_cselect_b32 s16, 0, s16
	s_add_i32 s17, s17, 0xc000
	s_cmp_eq_u32 s17, 0x24000
	s_cselect_b32 s17, 0, s17
	s_waitcnt vmcnt(6) lgkmcnt(0)
	s_barrier
	v_add_u32_e32 v106, s1, v84
	v_add_u32_e32 v110, s1, v77
	ds_read_b128 v[86:89], v106 offset:32768
	ds_read_b128 v[90:93], v106 offset:34816
	ds_read_b128 v[94:97], v110
	ds_read_b128 v[98:101], v110 offset:2048
	ds_read_b128 v[102:105], v106 offset:36864
	ds_read_b128 v[106:109], v106 offset:38912
	s_waitcnt lgkmcnt(0)
	v_mfma_f32_16x16x32_f16 v[60:63], v[86:89], v[94:97], v[60:63]
	v_add_u32_e32 v79, s1, v85
	v_mfma_f32_16x16x32_f16 v[56:59], v[90:93], v[94:97], v[56:59]
	v_mfma_f32_16x16x32_f16 v[52:55], v[102:105], v[94:97], v[52:55]
	s_mov_b32 m0, s19
	v_lshl_add_u64 v[112:113], v[74:75], 0, s[2:3]
	global_load_lds_dwordx4 v[112:113], off
	v_mfma_f32_16x16x32_f16 v[48:51], v[106:109], v[94:97], v[48:51]
	v_mfma_f32_16x16x32_f16 v[44:47], v[86:89], v[98:101], v[44:47]
	v_mfma_f32_16x16x32_f16 v[40:43], v[90:93], v[98:101], v[40:43]
	v_mfma_f32_16x16x32_f16 v[36:39], v[102:105], v[98:101], v[36:39]
	v_mfma_f32_16x16x32_f16 v[32:35], v[106:109], v[98:101], v[32:35]
	s_mov_b32 m0, s20
	v_lshl_add_u64 v[112:113], v[72:73], 0, s[2:3]
	global_load_lds_dwordx4 v[112:113], off
	ds_read_b128 v[94:97], v110 offset:4096
	ds_read_b128 v[98:101], v110 offset:6144
	v_add_u32_e32 v110, s1, v78
	s_waitcnt lgkmcnt(0)
	v_mfma_f32_16x16x32_f16 v[28:31], v[86:89], v[94:97], v[28:31]
	v_mfma_f32_16x16x32_f16 v[24:27], v[90:93], v[94:97], v[24:27]
	v_mfma_f32_16x16x32_f16 v[20:23], v[102:105], v[94:97], v[20:23]
	v_mfma_f32_16x16x32_f16 v[16:19], v[106:109], v[94:97], v[16:19]
	v_mfma_f32_16x16x32_f16 v[12:15], v[86:89], v[98:101], v[12:15]
	s_mov_b32 m0, s21
	v_lshl_add_u64 v[112:113], v[70:71], 0, s[2:3]
	global_load_lds_dwordx4 v[112:113], off
	v_mfma_f32_16x16x32_f16 v[8:11], v[90:93], v[98:101], v[8:11]
	ds_read_b128 v[86:89], v110 offset:32768
	ds_read_b128 v[90:93], v110 offset:34816
	v_mfma_f32_16x16x32_f16 v[0:3], v[102:105], v[98:101], v[0:3]
	v_mfma_f32_16x16x32_f16 v[4:7], v[106:109], v[98:101], v[4:7]
	ds_read_b128 v[94:97], v79
	ds_read_b128 v[98:101], v79 offset:2048
	ds_read_b128 v[102:105], v110 offset:36864
	ds_read_b128 v[106:109], v110 offset:38912
	s_waitcnt lgkmcnt(0)
	v_mfma_f32_16x16x32_f16 v[60:63], v[86:89], v[94:97], v[60:63]
	v_mfma_f32_16x16x32_f16 v[56:59], v[90:93], v[94:97], v[56:59]
	v_mfma_f32_16x16x32_f16 v[52:55], v[102:105], v[94:97], v[52:55]
	s_mov_b32 m0, s22
	v_lshl_add_u64 v[112:113], v[68:69], 0, s[2:3]
	global_load_lds_dwordx4 v[112:113], off
	v_mfma_f32_16x16x32_f16 v[48:51], v[106:109], v[94:97], v[48:51]
	v_mfma_f32_16x16x32_f16 v[44:47], v[86:89], v[98:101], v[44:47]
	v_mfma_f32_16x16x32_f16 v[40:43], v[90:93], v[98:101], v[40:43]
	v_mfma_f32_16x16x32_f16 v[36:39], v[102:105], v[98:101], v[36:39]
	v_mfma_f32_16x16x32_f16 v[32:35], v[106:109], v[98:101], v[32:35]
	s_mov_b32 m0, s23
	v_lshl_add_u64 v[112:113], v[66:67], 0, s[2:3]
	global_load_lds_dwordx4 v[112:113], off
	ds_read_b128 v[94:97], v79 offset:4096
	ds_read_b128 v[98:101], v79 offset:6144
	s_waitcnt lgkmcnt(0)
	v_mfma_f32_16x16x32_f16 v[28:31], v[86:89], v[94:97], v[28:31]
	v_mfma_f32_16x16x32_f16 v[24:27], v[90:93], v[94:97], v[24:27]
	v_mfma_f32_16x16x32_f16 v[20:23], v[102:105], v[94:97], v[20:23]
	v_mfma_f32_16x16x32_f16 v[16:19], v[106:109], v[94:97], v[16:19]
	v_mfma_f32_16x16x32_f16 v[12:15], v[86:89], v[98:101], v[12:15]
	s_mov_b32 m0, s24
	v_lshl_add_u64 v[112:113], v[64:65], 0, s[2:3]
	global_load_lds_dwordx4 v[112:113], off
	s_add_u32 s2, s2, 0x80
	s_addc_u32 s3, s3, 0
	s_cmpk_eq_i32 s2, 0xf80
	v_mfma_f32_16x16x32_f16 v[8:11], v[90:93], v[98:101], v[8:11]
	v_mfma_f32_16x16x32_f16 v[0:3], v[102:105], v[98:101], v[0:3]
	v_mfma_f32_16x16x32_f16 v[4:7], v[106:109], v[98:101], v[4:7]
	s_cbranch_scc0 .LBB1_1
	s_mov_b32 s1, 0
	s_waitcnt vmcnt(6) lgkmcnt(0)
	s_barrier
	v_add_u32_e32 v106, s1, v84
	v_add_u32_e32 v110, s1, v77
	ds_read_b128 v[86:89], v106 offset:32768
	ds_read_b128 v[90:93], v106 offset:34816
	ds_read_b128 v[94:97], v110
	ds_read_b128 v[98:101], v110 offset:2048
	ds_read_b128 v[102:105], v106 offset:36864
	ds_read_b128 v[106:109], v106 offset:38912
	s_waitcnt lgkmcnt(0)
	v_mfma_f32_16x16x32_f16 v[60:63], v[86:89], v[94:97], v[60:63]
	v_add_u32_e32 v79, s1, v85
	v_mfma_f32_16x16x32_f16 v[56:59], v[90:93], v[94:97], v[56:59]
	v_mfma_f32_16x16x32_f16 v[52:55], v[102:105], v[94:97], v[52:55]
	v_mfma_f32_16x16x32_f16 v[48:51], v[106:109], v[94:97], v[48:51]
	v_mfma_f32_16x16x32_f16 v[44:47], v[86:89], v[98:101], v[44:47]
	v_mfma_f32_16x16x32_f16 v[40:43], v[90:93], v[98:101], v[40:43]
	v_mfma_f32_16x16x32_f16 v[36:39], v[102:105], v[98:101], v[36:39]
	v_mfma_f32_16x16x32_f16 v[32:35], v[106:109], v[98:101], v[32:35]
	ds_read_b128 v[94:97], v110 offset:4096
	ds_read_b128 v[98:101], v110 offset:6144
	v_add_u32_e32 v110, s1, v78
	s_waitcnt lgkmcnt(0)
	v_mfma_f32_16x16x32_f16 v[28:31], v[86:89], v[94:97], v[28:31]
	v_mfma_f32_16x16x32_f16 v[24:27], v[90:93], v[94:97], v[24:27]
	v_mfma_f32_16x16x32_f16 v[20:23], v[102:105], v[94:97], v[20:23]
	v_mfma_f32_16x16x32_f16 v[16:19], v[106:109], v[94:97], v[16:19]
	v_mfma_f32_16x16x32_f16 v[12:15], v[86:89], v[98:101], v[12:15]
	v_mfma_f32_16x16x32_f16 v[8:11], v[90:93], v[98:101], v[8:11]
	ds_read_b128 v[86:89], v110 offset:32768
	ds_read_b128 v[90:93], v110 offset:34816
	v_mfma_f32_16x16x32_f16 v[0:3], v[102:105], v[98:101], v[0:3]
	v_mfma_f32_16x16x32_f16 v[4:7], v[106:109], v[98:101], v[4:7]
	ds_read_b128 v[94:97], v79
	ds_read_b128 v[98:101], v79 offset:2048
	ds_read_b128 v[102:105], v110 offset:36864
	ds_read_b128 v[106:109], v110 offset:38912
	s_waitcnt lgkmcnt(0)
	v_mfma_f32_16x16x32_f16 v[60:63], v[86:89], v[94:97], v[60:63]
	v_mfma_f32_16x16x32_f16 v[56:59], v[90:93], v[94:97], v[56:59]
	v_mfma_f32_16x16x32_f16 v[52:55], v[102:105], v[94:97], v[52:55]
	v_mfma_f32_16x16x32_f16 v[48:51], v[106:109], v[94:97], v[48:51]
	v_mfma_f32_16x16x32_f16 v[44:47], v[86:89], v[98:101], v[44:47]
	v_mfma_f32_16x16x32_f16 v[40:43], v[90:93], v[98:101], v[40:43]
	v_mfma_f32_16x16x32_f16 v[36:39], v[102:105], v[98:101], v[36:39]
	v_mfma_f32_16x16x32_f16 v[32:35], v[106:109], v[98:101], v[32:35]
	ds_read_b128 v[94:97], v79 offset:4096
	ds_read_b128 v[98:101], v79 offset:6144
	s_waitcnt lgkmcnt(0)
	v_mfma_f32_16x16x32_f16 v[28:31], v[86:89], v[94:97], v[28:31]
	v_mfma_f32_16x16x32_f16 v[24:27], v[90:93], v[94:97], v[24:27]
	v_mfma_f32_16x16x32_f16 v[20:23], v[102:105], v[94:97], v[20:23]
	v_mfma_f32_16x16x32_f16 v[16:19], v[106:109], v[94:97], v[16:19]
	v_mfma_f32_16x16x32_f16 v[12:15], v[86:89], v[98:101], v[12:15]
	v_mfma_f32_16x16x32_f16 v[8:11], v[90:93], v[98:101], v[8:11]
	v_mfma_f32_16x16x32_f16 v[0:3], v[102:105], v[98:101], v[0:3]
	v_mfma_f32_16x16x32_f16 v[4:7], v[106:109], v[98:101], v[4:7]
	s_add_i32 s1, 0, 0xc000
	v_add_u32_e32 v64, s1, v84
	s_waitcnt vmcnt(0)
	s_waitcnt vmcnt(0)
	s_barrier
	ds_read_b128 v[86:89], v64 offset:32768
	v_add_u32_e32 v94, 0, v77
	ds_read_b128 v[72:75], v64 offset:34816
	ds_read_b128 v[76:79], v94 offset:49152
	ds_read_b128 v[90:93], v94 offset:51200
	ds_read_b128 v[68:71], v64 offset:36864
	ds_read_b128 v[64:67], v64 offset:38912
	s_waitcnt lgkmcnt(3)
	v_mfma_f32_16x16x32_f16 v[60:63], v[86:89], v[76:79], v[60:63]
	v_lshl_add_u32 v81, v81, 6, s0
	v_or_b32_e32 v80, v81, v80
	v_ashrrev_i32_e32 v81, 31, v80
	v_mfma_f32_16x16x32_f16 v[56:59], v[72:75], v[76:79], v[56:59]
	v_xor_b32_e32 v84, 0x8040, v84
	v_lshl_add_u64 v[100:101], v[80:81], 2, s[10:11]
	v_add_u32_e32 v96, 0, v85
	s_waitcnt lgkmcnt(1)
	v_mfma_f32_16x16x32_f16 v[52:55], v[68:71], v[76:79], v[52:55]
	v_lshlrev_b32_e32 v82, 6, v82
	v_mov_b32_e32 v105, 0x3727c5ac
	s_mov_b32 s2, 0x800000
	s_waitcnt lgkmcnt(0)
	v_mfma_f32_16x16x32_f16 v[48:51], v[64:67], v[76:79], v[48:51]
	v_mfma_f32_16x16x32_f16 v[44:47], v[86:89], v[90:93], v[44:47]
	v_mfma_f32_16x16x32_f16 v[40:43], v[72:75], v[90:93], v[40:43]
	v_mfma_f32_16x16x32_f16 v[36:39], v[68:71], v[90:93], v[36:39]
	v_mfma_f32_16x16x32_f16 v[32:35], v[64:67], v[90:93], v[32:35]
	ds_read_b128 v[90:93], v94 offset:53248
	ds_read_b128 v[76:79], v94 offset:55296
	global_load_dword v102, v[100:101], off
	global_load_dword v103, v[100:101], off offset:64
	global_load_dword v104, v[100:101], off offset:128
	s_waitcnt lgkmcnt(1)
	v_mfma_f32_16x16x32_f16 v[28:31], v[86:89], v[90:93], v[28:31]
	s_waitcnt lgkmcnt(0)
	v_mfma_f32_16x16x32_f16 v[12:15], v[86:89], v[76:79], v[12:15]
	v_add_u32_e32 v88, s1, v84
	v_mfma_f32_16x16x32_f16 v[24:27], v[72:75], v[90:93], v[24:27]
	v_mfma_f32_16x16x32_f16 v[20:23], v[68:71], v[90:93], v[20:23]
	v_mfma_f32_16x16x32_f16 v[16:19], v[64:67], v[90:93], v[16:19]
	v_lshlrev_b32_e32 v92, 2, v83
	v_or3_b32 v82, v82, v92, s12
	v_mov_b32_e32 v83, 0
	v_mfma_f32_16x16x32_f16 v[8:11], v[72:75], v[76:79], v[8:11]
	ds_read_b128 v[72:75], v88
	v_lshlrev_b32_e32 v82, 2, v82
	v_mfma_f32_16x16x32_f16 v[0:3], v[68:71], v[76:79], v[0:3]
	ds_read_b128 v[68:71], v96 offset:49152
	ds_read_b128 v[84:87], v88 offset:2048
	v_mfma_f32_16x16x32_f16 v[4:7], v[64:67], v[76:79], v[4:7]
	ds_read_b128 v[64:67], v96 offset:51200
	ds_read_b128 v[76:79], v88 offset:4096
	ds_read_b128 v[88:91], v88 offset:6144
	ds_read_b128 v[92:95], v96 offset:53248
	ds_read_b128 v[96:99], v96 offset:55296
	s_waitcnt lgkmcnt(6)
	v_mfma_f32_16x16x32_f16 v[60:63], v[72:75], v[68:71], v[60:63]
	s_waitcnt lgkmcnt(5)
	v_mfma_f32_16x16x32_f16 v[56:59], v[84:87], v[68:71], v[56:59]
	s_waitcnt lgkmcnt(3)
	v_mfma_f32_16x16x32_f16 v[52:55], v[76:79], v[68:71], v[52:55]
	s_waitcnt lgkmcnt(2)
	v_mfma_f32_16x16x32_f16 v[48:51], v[88:91], v[68:71], v[48:51]
	global_load_dword v71, v[100:101], off offset:192
	v_lshlrev_b64 v[68:69], 12, v[80:81]
	v_lshl_add_u64 v[68:69], s[8:9], 0, v[68:69]
	v_lshl_add_u64 v[68:69], v[68:69], 0, v[82:83]
	v_mfma_f32_16x16x32_f16 v[32:35], v[88:91], v[64:67], v[32:35]
	s_waitcnt vmcnt(3)
	v_fmamk_f32 v70, v102, 0x3a000000, v105
	v_mul_f32_e32 v100, 0x4b800000, v70
	v_cmp_gt_f32_e32 vcc, s2, v70
	s_waitcnt vmcnt(2)
	v_fmamk_f32 v81, v103, 0x3a000000, v105
	v_mul_f32_e32 v101, 0x4b800000, v81
	v_cndmask_b32_e32 v70, v70, v100, vcc
	v_rsq_f32_e32 v70, v70
	v_cmp_gt_f32_e64 s[0:1], s2, v81
	s_waitcnt lgkmcnt(1)
	v_mfma_f32_16x16x32_f16 v[20:23], v[76:79], v[92:95], v[20:23]
	v_mul_f32_e32 v100, 0x45800000, v70
	v_cndmask_b32_e64 v81, v81, v101, s[0:1]
	v_rsq_f32_e32 v81, v81
	v_cndmask_b32_e32 v70, v70, v100, vcc
	v_mul_f32_e32 v70, 0x3b000000, v70
	v_mfma_f32_16x16x32_f16 v[16:19], v[88:91], v[92:95], v[16:19]
	v_mul_f32_e32 v101, 0x45800000, v81
	v_cndmask_b32_e64 v81, v81, v101, s[0:1]
	v_mul_f32_e32 v100, 0x3b000000, v81
	v_pk_mul_f32 v[34:35], v[100:101], v[34:35] op_sel_hi:[0,1]
	v_pk_mul_f32 v[32:33], v[100:101], v[32:33] op_sel_hi:[0,1]
	s_waitcnt lgkmcnt(0)
	v_mfma_f32_16x16x32_f16 v[0:3], v[76:79], v[96:99], v[0:3]
	s_waitcnt vmcnt(0)
	v_pk_mul_f32 v[62:63], v[70:71], v[62:63] op_sel_hi:[0,1]
	v_pk_mul_f32 v[60:61], v[70:71], v[60:61] op_sel_hi:[0,1]
	v_pk_mul_f32 v[48:49], v[70:71], v[48:49] op_sel_hi:[0,1]
	v_pk_mul_f32 v[58:59], v[70:71], v[58:59] op_sel_hi:[0,1]
	v_pk_mul_f32 v[56:57], v[70:71], v[56:57] op_sel_hi:[0,1]
	v_pk_mul_f32 v[54:55], v[70:71], v[54:55] op_sel_hi:[0,1]
	v_pk_mul_f32 v[52:53], v[70:71], v[52:53] op_sel_hi:[0,1]
	v_pk_mul_f32 v[50:51], v[70:71], v[50:51] op_sel_hi:[0,1]
	global_store_dwordx4 v[68:69], v[60:63], off nt
	global_store_dwordx4 v[68:69], v[56:59], off offset:64 nt
	global_store_dwordx4 v[68:69], v[52:55], off offset:128 nt
	global_store_dwordx4 v[68:69], v[48:51], off offset:192 nt
	v_mfma_f32_16x16x32_f16 v[44:47], v[72:75], v[64:67], v[44:47]
	s_nop 0
	v_or_b32_e32 v48, 16, v80
	v_ashrrev_i32_e32 v49, 31, v48
	v_lshlrev_b64 v[48:49], 12, v[48:49]
	v_lshl_add_u64 v[48:49], s[8:9], 0, v[48:49]
	v_lshl_add_u64 v[48:49], v[48:49], 0, v[82:83]
	global_store_dwordx4 v[48:49], v[32:35], off offset:192 nt
	v_mfma_f32_16x16x32_f16 v[40:43], v[84:87], v[64:67], v[40:43]
	v_mul_f32_e64 v46, v100, v46
	v_mul_f32_e64 v47, v100, v47
	v_fmamk_f32 v32, v104, 0x3a000000, v105
	v_mul_f32_e32 v33, 0x4b800000, v32
	v_cmp_gt_f32_e32 vcc, s2, v32
	v_fmac_f32_e32 v105, 0x3a000000, v71
	v_mfma_f32_16x16x32_f16 v[36:39], v[76:79], v[64:67], v[36:39]
	v_cndmask_b32_e32 v32, v32, v33, vcc
	v_rsq_f32_e32 v34, v32
	v_or_b32_e32 v32, 32, v80
	v_ashrrev_i32_e32 v33, 31, v32
	v_lshlrev_b64 v[32:33], 12, v[32:33]
	v_mul_f32_e32 v35, 0x45800000, v34
	v_cndmask_b32_e32 v34, v34, v35, vcc
	v_mul_f32_e32 v34, 0x3b000000, v34
	v_lshl_add_u64 v[32:33], s[8:9], 0, v[32:33]
	v_lshl_add_u64 v[32:33], v[32:33], 0, v[82:83]
	v_pk_mul_f32 v[22:23], v[34:35], v[22:23] op_sel_hi:[0,1]
	v_pk_mul_f32 v[20:21], v[34:35], v[20:21] op_sel_hi:[0,1]
	global_store_dwordx4 v[32:33], v[20:23], off offset:128 nt
	v_cmp_gt_f32_e32 vcc, s2, v105
	v_pk_mul_f32 v[18:19], v[34:35], v[18:19] op_sel_hi:[0,1]
	v_mul_f32_e32 v20, 0x4b800000, v105
	v_cndmask_b32_e32 v20, v105, v20, vcc
	v_rsq_f32_e32 v20, v20
	v_pk_mul_f32 v[16:17], v[34:35], v[16:17] op_sel_hi:[0,1]
	global_store_dwordx4 v[32:33], v[16:19], off offset:192 nt
	v_mfma_f32_16x16x32_f16 v[28:31], v[72:75], v[92:95], v[28:31]
	v_mul_f32_e64 v44, v100, v44
	v_mul_f32_e64 v45, v100, v45
	v_or_b32_e32 v16, 48, v80
	v_ashrrev_i32_e32 v17, 31, v16
	v_mfma_f32_16x16x32_f16 v[24:27], v[84:87], v[92:95], v[24:27]
	v_mul_f32_e32 v18, 0x45800000, v20
	v_cndmask_b32_e32 v18, v20, v18, vcc
	v_lshlrev_b64 v[16:17], 12, v[16:17]
	v_mfma_f32_16x16x32_f16 v[12:15], v[72:75], v[96:99], v[12:15]
	v_mul_f32_e32 v18, 0x3b000000, v18
	v_lshl_add_u64 v[16:17], s[8:9], 0, v[16:17]
	v_lshl_add_u64 v[16:17], v[16:17], 0, v[82:83]
	v_mfma_f32_16x16x32_f16 v[8:11], v[84:87], v[96:99], v[8:11]
	v_mul_f32_e64 v2, v18, v2
	v_mul_f32_e64 v3, v18, v3
	v_pk_mul_f32 v[0:1], v[18:19], v[0:1] op_sel_hi:[0,1]
	v_pk_mul_f32 v[42:43], v[100:101], v[42:43] op_sel_hi:[0,1]
	v_mfma_f32_16x16x32_f16 v[4:7], v[88:91], v[96:99], v[4:7]
	v_mul_f32_e64 v40, v100, v40
	v_mul_f32_e64 v41, v100, v41
	v_pk_mul_f32 v[38:39], v[100:101], v[38:39] op_sel_hi:[0,1]
	v_pk_mul_f32 v[36:37], v[100:101], v[36:37] op_sel_hi:[0,1]
	v_pk_mul_f32 v[30:31], v[34:35], v[30:31] op_sel_hi:[0,1]
	v_pk_mul_f32 v[28:29], v[34:35], v[28:29] op_sel_hi:[0,1]
	v_pk_mul_f32 v[26:27], v[34:35], v[26:27] op_sel_hi:[0,1]
	v_pk_mul_f32 v[24:25], v[34:35], v[24:25] op_sel_hi:[0,1]
	v_pk_mul_f32 v[14:15], v[18:19], v[14:15] op_sel_hi:[0,1]
	v_pk_mul_f32 v[12:13], v[18:19], v[12:13] op_sel_hi:[0,1]
	v_pk_mul_f32 v[10:11], v[18:19], v[10:11] op_sel_hi:[0,1]
	v_pk_mul_f32 v[8:9], v[18:19], v[8:9] op_sel_hi:[0,1]
	global_store_dwordx4 v[16:17], v[0:3], off offset:128 nt
	global_store_dwordx4 v[48:49], v[44:47], off nt
	global_store_dwordx4 v[48:49], v[40:43], off offset:64 nt
	v_pk_mul_f32 v[2:3], v[18:19], v[6:7] op_sel_hi:[0,1]
	v_pk_mul_f32 v[0:1], v[18:19], v[4:5] op_sel_hi:[0,1]
	global_store_dwordx4 v[48:49], v[36:39], off offset:128 nt
	global_store_dwordx4 v[32:33], v[28:31], off nt
	global_store_dwordx4 v[32:33], v[24:27], off offset:64 nt
	global_store_dwordx4 v[16:17], v[12:15], off nt
	global_store_dwordx4 v[16:17], v[8:11], off offset:64 nt
	global_store_dwordx4 v[16:17], v[0:3], off offset:192 nt
	s_endpgm

	.amdhsa_kernel _Z13gemm2b_kernelPKDF16_S0_PfPKf
		.amdhsa_group_segment_fixed_size 49152
		.amdhsa_private_segment_fixed_size 0
		.amdhsa_kernarg_size 32
		.amdhsa_user_sgpr_count 2
		.amdhsa_user_sgpr_dispatch_ptr 0
		.amdhsa_user_sgpr_queue_ptr 0
		.amdhsa_user_sgpr_kernarg_segment_ptr 1
		.amdhsa_user_sgpr_dispatch_id 0
		.amdhsa_user_sgpr_kernarg_preload_length 0
		.amdhsa_user_sgpr_kernarg_preload_offset 0
		.amdhsa_user_sgpr_private_segment_size 0
		.amdhsa_uses_dynamic_stack 0
		.amdhsa_enable_private_segment 0
		.amdhsa_system_sgpr_workgroup_id_x 1
		.amdhsa_system_sgpr_workgroup_id_y 0
		.amdhsa_system_sgpr_workgroup_id_z 0
		.amdhsa_system_sgpr_workgroup_info 0
		.amdhsa_system_vgpr_workitem_id 0
		.amdhsa_next_free_vgpr 114
		.amdhsa_next_free_sgpr 25
		.amdhsa_accum_offset 116
		.amdhsa_reserve_vcc 1
		.amdhsa_float_round_mode_32 0
		.amdhsa_float_round_mode_16_64 0
		.amdhsa_float_denorm_mode_32 3
		.amdhsa_float_denorm_mode_16_64 3
		.amdhsa_dx10_clamp 1
		.amdhsa_ieee_mode 1
		.amdhsa_fp16_overflow 0
		.amdhsa_tg_split 0
		.amdhsa_exception_fp_ieee_invalid_op 0
		.amdhsa_exception_fp_denorm_src 0
		.amdhsa_exception_fp_ieee_div_zero 0
		.amdhsa_exception_fp_ieee_overflow 0
		.amdhsa_exception_fp_ieee_underflow 0
		.amdhsa_exception_fp_ieee_inexact 0
		.amdhsa_exception_int_div_zero 0
	.end_amdhsa_kernel

amdhsa.kernels:
  - .agpr_count:     0
    .args:
      - .actual_access:  read_only
        .address_space:  global
        .offset:         0
        .size:           8
        .value_kind:     global_buffer
      - .actual_access:  read_only
        .address_space:  global
        .offset:         8
        .size:           8
        .value_kind:     global_buffer
      - .actual_access:  read_only
        .address_space:  global
        .offset:         16
        .size:           8
        .value_kind:     global_buffer
      - .actual_access:  read_only
        .address_space:  global
        .offset:         24
        .size:           8
        .value_kind:     global_buffer
      - .actual_access:  write_only
        .address_space:  global
        .offset:         32
        .size:           8
        .value_kind:     global_buffer
      - .actual_access:  write_only
        .address_space:  global
        .offset:         40
        .size:           8
        .value_kind:     global_buffer
      - .actual_access:  write_only
        .address_space:  global
        .offset:         48
        .size:           8
        .value_kind:     global_buffer
      - .actual_access:  write_only
        .address_space:  global
        .offset:         56
        .size:           8
        .value_kind:     global_buffer
    .group_segment_fixed_size: 16640
    .kernarg_segment_align: 8
    .kernarg_segment_size: 64
    .language:       OpenCL C
    .language_version:
      - 2
      - 0
    .max_flat_workgroup_size: 256
    .name:           _Z11prep_kernelPKfS0_S0_S0_PDF16_S1_S1_Pf
    .private_segment_fixed_size: 0
    .sgpr_count:     18
    .sgpr_spill_count: 0
    .symbol:         _Z11prep_kernelPKfS0_S0_S0_PDF16_S1_S1_Pf.kd
    .uniform_work_group_size: 1
    .uses_dynamic_stack: false
    .vgpr_count:     42
    .vgpr_spill_count: 0
    .wavefront_size: 64
  - .agpr_count:     0
    .args:
      - .address_space:  global
        .offset:         0
        .size:           8
        .value_kind:     global_buffer
      - .address_space:  global
        .offset:         8
        .size:           8
        .value_kind:     global_buffer
      - .actual_access:  write_only
        .address_space:  global
        .offset:         16
        .size:           8
        .value_kind:     global_buffer
      - .actual_access:  read_only
        .address_space:  global
        .offset:         24
        .size:           8
        .value_kind:     global_buffer
    .group_segment_fixed_size: 49152
    .kernarg_segment_align: 8
    .kernarg_segment_size: 32
    .language:       OpenCL C
    .language_version:
      - 2
      - 0
    .max_flat_workgroup_size: 512
    .name:           _Z13gemm2b_kernelPKDF16_S0_PfPKf
    .private_segment_fixed_size: 0
    .sgpr_count:     31
    .sgpr_spill_count: 0
    .symbol:         _Z13gemm2b_kernelPKDF16_S0_PfPKf.kd
    .uniform_work_group_size: 1
    .uses_dynamic_stack: false
    .vgpr_count:     111
    .vgpr_spill_count: 0
    .wavefront_size: 64
  - .agpr_count:     0
    .args:
      - .address_space:  global
        .offset:         0
        .size:           8
        .value_kind:     global_buffer
      - .address_space:  global
        .offset:         8
        .size:           8
        .value_kind:     global_buffer
      - .actual_access:  write_only
        .address_space:  global
        .offset:         16
        .size:           8
        .value_kind:     global_buffer
      - .actual_access:  write_only
        .address_space:  global
        .offset:         24
        .size:           8
        .value_kind:     global_buffer
    .group_segment_fixed_size: 0
    .kernarg_segment_align: 8
    .kernarg_segment_size: 32
    .language:       OpenCL C
    .language_version:
      - 2
      - 0
    .max_flat_workgroup_size: 512
    .name:           _Z12gemm8_kernelPKDF16_S0_PDF16_S1_
    .private_segment_fixed_size: 0
    .sgpr_count:     58
    .sgpr_spill_count: 0
    .symbol:         _Z12gemm8_kernelPKDF16_S0_PDF16_S1_.kd
    .uniform_work_group_size: 1
    .uses_dynamic_stack: false
    .vgpr_count:     220
    .vgpr_spill_count: 0
    .wavefront_size: 64
  - .agpr_count:     0
    .args:
      - .actual_access:  read_only
        .address_space:  global
        .offset:         0
        .size:           8
        .value_kind:     global_buffer
      - .actual_access:  read_only
        .address_space:  global
        .offset:         8
        .size:           8
        .value_kind:     global_buffer
      - .actual_access:  read_only
        .address_space:  global
        .offset:         16
        .size:           8
        .value_kind:     global_buffer
      - .actual_access:  read_only
        .address_space:  global
        .offset:         24
        .size:           8
        .value_kind:     global_buffer
      - .actual_access:  write_only
        .address_space:  global
        .offset:         32
        .size:           8
        .value_kind:     global_buffer
      - .actual_access:  write_only
        .address_space:  global
        .offset:         40
        .size:           8
        .value_kind:     global_buffer
      - .actual_access:  read_only
        .address_space:  global
        .offset:         48
        .size:           8
        .value_kind:     global_buffer
      - .actual_access:  read_only
        .address_space:  global
        .offset:         56
        .size:           8
        .value_kind:     global_buffer
      - .actual_access:  read_only
        .address_space:  global
        .offset:         64
        .size:           8
        .value_kind:     global_buffer
      - .actual_access:  write_only
        .address_space:  global
        .offset:         72
        .size:           8
        .value_kind:     global_buffer
      - .actual_access:  write_only
        .address_space:  global
        .offset:         80
        .size:           8
        .value_kind:     global_buffer
      - .actual_access:  write_only
        .address_space:  global
        .offset:         88
        .size:           8
        .value_kind:     global_buffer
      - .actual_access:  write_only
        .address_space:  global
        .offset:         96
        .size:           8
        .value_kind:     global_buffer
    .group_segment_fixed_size: 17952
    .kernarg_segment_align: 8
    .kernarg_segment_size: 104
    .language:       OpenCL C
    .language_version:
      - 2
      - 0
    .max_flat_workgroup_size: 256
    .name:           _Z13convdt_kernelPKDF16_S0_PKfS2_PDF16_S3_S2_S2_S2_PfS4_S4_S4_
    .private_segment_fixed_size: 0
    .sgpr_count:     26
    .sgpr_spill_count: 0
    .symbol:         _Z13convdt_kernelPKDF16_S0_PKfS2_PDF16_S3_S2_S2_S2_PfS4_S4_S4_.kd
    .uniform_work_group_size: 1
    .uses_dynamic_stack: false
    .vgpr_count:     88
    .vgpr_spill_count: 0
    .wavefront_size: 64
  - .agpr_count:     0
    .args:
      - .actual_access:  read_only
        .address_space:  global
        .offset:         0
        .size:           8
        .value_kind:     global_buffer
      - .actual_access:  read_only
        .address_space:  global
        .offset:         8
        .size:           8
        .value_kind:     global_buffer
      - .actual_access:  read_only
        .address_space:  global
        .offset:         16
        .size:           8
        .value_kind:     global_buffer
      - .actual_access:  write_only
        .address_space:  global
        .offset:         24
        .size:           8
        .value_kind:     global_buffer
    .group_segment_fixed_size: 34816
    .kernarg_segment_align: 8
    .kernarg_segment_size: 32
    .language:       OpenCL C
    .language_version:
      - 2
      - 0
    .max_flat_workgroup_size: 256
    .name:           _Z11sloc_kernelPKDF16_PKfS2_PDF16_
    .private_segment_fixed_size: 0
    .sgpr_count:     28
    .sgpr_spill_count: 0
    .symbol:         _Z11sloc_kernelPKDF16_PKfS2_PDF16_.kd
    .uniform_work_group_size: 1
    .uses_dynamic_stack: false
    .vgpr_count:     120
    .vgpr_spill_count: 0
    .wavefront_size: 64
  - .agpr_count:     64
    .args:
      - .actual_access:  read_only
        .address_space:  global
        .offset:         0
        .size:           8
        .value_kind:     global_buffer
      - .address_space:  global
        .offset:         8
        .size:           8
        .value_kind:     global_buffer
      - .actual_access:  read_only
        .address_space:  global
        .offset:         16
        .size:           8
        .value_kind:     global_buffer
      - .actual_access:  write_only
        .address_space:  global
        .offset:         24
        .size:           8
        .value_kind:     global_buffer
    .group_segment_fixed_size: 0
    .kernarg_segment_align: 8
    .kernarg_segment_size: 32
    .language:       OpenCL C
    .language_version:
      - 2
      - 0
    .max_flat_workgroup_size: 256
    .name:           _Z12spass_kernelPKfPDF16_PKDF16_S1_
    .private_segment_fixed_size: 0
    .sgpr_count:     21
    .sgpr_spill_count: 0
    .symbol:         _Z12spass_kernelPKfPDF16_PKDF16_S1_.kd
    .uniform_work_group_size: 1
    .uses_dynamic_stack: false
    .vgpr_count:     180
    .vgpr_spill_count: 0
    .wavefront_size: 64
  - .agpr_count:     0
    .args:
      - .actual_access:  read_only
        .address_space:  global
        .offset:         0
        .size:           8
        .value_kind:     global_buffer
      - .actual_access:  read_only
        .address_space:  global
        .offset:         8
        .size:           8
        .value_kind:     global_buffer
      - .actual_access:  read_only
        .address_space:  global
        .offset:         16
        .size:           8
        .value_kind:     global_buffer
      - .actual_access:  read_only
        .address_space:  global
        .offset:         24
        .size:           8
        .value_kind:     global_buffer
      - .actual_access:  read_only
        .address_space:  global
        .offset:         32
        .size:           8
        .value_kind:     global_buffer
      - .actual_access:  read_only
        .address_space:  global
        .offset:         40
        .size:           8
        .value_kind:     global_buffer
      - .actual_access:  read_only
        .address_space:  global
        .offset:         48
        .size:           8
        .value_kind:     global_buffer
      - .actual_access:  read_only
        .address_space:  global
        .offset:         56
        .size:           8
        .value_kind:     global_buffer
      - .actual_access:  read_only
        .address_space:  global
        .offset:         64
        .size:           8
        .value_kind:     global_buffer
      - .actual_access:  write_only
        .address_space:  global
        .offset:         72
        .size:           8
        .value_kind:     global_buffer
      - .address_space:  global
        .offset:         80
        .size:           8
        .value_kind:     global_buffer
      - .actual_access:  read_only
        .address_space:  global
        .offset:         88
        .size:           8
        .value_kind:     global_buffer
    .group_segment_fixed_size: 54272
    .kernarg_segment_align: 8
    .kernarg_segment_size: 96
    .language:       OpenCL C
    .language_version:
      - 2
      - 0
    .max_flat_workgroup_size: 256
    .name:           _Z11scan_kernelPKDF16_S0_S0_S0_S0_PKfS2_S2_S2_PDF16_PfS4_
    .private_segment_fixed_size: 0
    .sgpr_count:     106
    .sgpr_spill_count: 56
    .symbol:         _Z11scan_kernelPKDF16_S0_S0_S0_S0_PKfS2_S2_S2_PDF16_PfS4_.kd
    .uniform_work_group_size: 1
    .uses_dynamic_stack: false
    .vgpr_count:     243
    .vgpr_spill_count: 0
    .wavefront_size: 64
  - .agpr_count:     0
    .args:
      - .actual_access:  read_only
        .address_space:  global
        .offset:         0
        .size:           8
        .value_kind:     global_buffer
      - .address_space:  global
        .offset:         8
        .size:           8
        .value_kind:     global_buffer
      - .address_space:  global
        .offset:         16
        .size:           8
        .value_kind:     global_buffer
      - .actual_access:  read_only
        .address_space:  global
        .offset:         24
        .size:           8
        .value_kind:     global_buffer
      - .address_space:  global
        .offset:         32
        .size:           8
        .value_kind:     global_buffer
      - .address_space:  global
        .offset:         40
        .size:           8
        .value_kind:     global_buffer
      - .address_space:  global
        .offset:         48
        .size:           8
        .value_kind:     global_buffer
      - .actual_access:  read_only
        .address_space:  global
        .offset:         56
        .size:           8
        .value_kind:     global_buffer
      - .actual_access:  read_only
        .address_space:  global
        .offset:         64
        .size:           8
        .value_kind:     global_buffer
      - .actual_access:  write_only
        .address_space:  global
        .offset:         72
        .size:           8
        .value_kind:     global_buffer
      - .address_space:  global
        .offset:         80
        .size:           8
        .value_kind:     global_buffer
      - .actual_access:  read_only
        .address_space:  global
        .offset:         88
        .size:           8
        .value_kind:     global_buffer
    .group_segment_fixed_size: 0
    .kernarg_segment_align: 8
    .kernarg_segment_size: 96
    .language:       OpenCL C
    .language_version:
      - 2
      - 0
    .max_flat_workgroup_size: 512
    .name:           _Z12scan2_kernelPKDF16_S0_S0_S0_S0_PKfS2_S2_S2_PDF16_PfS4_
    .private_segment_fixed_size: 0
    .sgpr_count:     106
    .sgpr_spill_count: 53
    .symbol:         _Z12scan2_kernelPKDF16_S0_S0_S0_S0_PKfS2_S2_S2_PDF16_PfS4_.kd
    .uniform_work_group_size: 1
    .uses_dynamic_stack: false
    .vgpr_count:     240
    .vgpr_spill_count: 0
    .wavefront_size: 64
  - .agpr_count:     64
    .args:
      - .address_space:  global
        .offset:         0
        .size:           8
        .value_kind:     global_buffer
      - .address_space:  global
        .offset:         8
        .size:           8
        .value_kind:     global_buffer
      - .offset:         16
        .size:           4
        .value_kind:     by_value
      - .offset:         20
        .size:           4
        .value_kind:     by_value
      - .offset:         24
        .size:           4
        .value_kind:     by_value
      - .actual_access:  write_only
        .address_space:  global
        .offset:         32
        .size:           8
        .value_kind:     global_buffer
      - .actual_access:  write_only
        .address_space:  global
        .offset:         40
        .size:           8
        .value_kind:     global_buffer
      - .actual_access:  read_only
        .address_space:  global
        .offset:         48
        .size:           8
        .value_kind:     global_buffer
      - .offset:         56
        .size:           4
        .value_kind:     by_value
    .group_segment_fixed_size: 131072
    .kernarg_segment_align: 8
    .kernarg_segment_size: 60
    .language:       OpenCL C
    .language_version:
      - 2
      - 0
    .max_flat_workgroup_size: 256
    .name:           _Z11gemm_kernelILi1EEvPKDF16_S1_iiiPDF16_PfPKfi
    .private_segment_fixed_size: 0
    .sgpr_count:     27
    .sgpr_spill_count: 0
    .symbol:         _Z11gemm_kernelILi1EEvPKDF16_S1_iiiPDF16_PfPKfi.kd
    .uniform_work_group_size: 1
    .uses_dynamic_stack: false
    .vgpr_count:     208
    .vgpr_spill_count: 0
    .wavefront_size: 64
